# s3 + W_out epilogue: second half-tile residual pieces requested together with the first half
# baseline (speedup 1.0000x reference)
.LBB0_999:
	v_lshl_add_u32 v158, s18, 8, v153
	s_lshl_b32 s9, s19, 8
	s_ashr_i32 s11, s9, 31
	v_ashrrev_i32_e32 v159, 31, v158
	v_mov_b32_e32 v131, s11
	v_or_b32_e32 v130, s9, v152
	v_lshlrev_b64 v[132:133], 11, v[158:159]
	v_lshl_add_u64 v[132:133], s[4:5], 0, v[132:133]
	v_lshlrev_b64 v[160:161], 1, v[130:131]
	v_lshl_add_u64 v[178:179], v[132:133], 0, v[160:161]
	global_load_dwordx4 v[174:177], v[178:179], off
	global_load_dwordx4 v[200:203], v[178:179], off offset:256
	s_mov_b32 s18, 0x8000
	v_add_co_u32_e32 v168, vcc, s18, v178
	s_mov_b32 s9, 0x10000
	s_nop 0
	v_addc_co_u32_e32 v169, vcc, 0, v179, vcc
	global_load_dwordx4 v[204:207], v[168:169], off
	global_load_dwordx4 v[146:149], v[168:169], off offset:256
	v_add_co_u32_e32 v166, vcc, s9, v178
	s_mov_b32 s11, 0x18000
	s_nop 0
	v_addc_co_u32_e32 v167, vcc, 0, v179, vcc
	global_load_dwordx4 v[142:145], v[166:167], off
	global_load_dwordx4 v[138:141], v[166:167], off offset:256
	v_add_co_u32_e32 v164, vcc, s11, v178
	v_addc_co_u32_e32 v165, vcc, 0, v179, vcc
	global_load_dwordx4 v[134:137], v[164:165], off
	global_load_dwordx4 v[130:133], v[164:165], off offset:256
	v_add_co_u32_e32 v242, vcc, 0x40000, v178
	s_nop 1
	v_addc_co_u32_e32 v243, vcc, 0, v179, vcc
	global_load_dwordx4 v[210:213], v[242:243], off
	global_load_dwordx4 v[214:217], v[242:243], off offset:256
	v_add_co_u32_e32 v244, vcc, 0x40000, v168
	s_nop 1
	v_addc_co_u32_e32 v245, vcc, 0, v169, vcc
	global_load_dwordx4 v[218:221], v[244:245], off
	global_load_dwordx4 v[222:225], v[244:245], off offset:256
	v_add_co_u32_e32 v246, vcc, 0x40000, v166
	s_nop 1
	v_addc_co_u32_e32 v247, vcc, 0, v167, vcc
	global_load_dwordx4 v[226:229], v[246:247], off
	global_load_dwordx4 v[230:233], v[246:247], off offset:256
	v_add_co_u32_e32 v248, vcc, 0x40000, v164
	s_nop 1
	v_addc_co_u32_e32 v249, vcc, 0, v165, vcc
	global_load_dwordx4 v[234:237], v[248:249], off
	global_load_dwordx4 v[238:241], v[248:249], off offset:256
	s_waitcnt vmcnt(8)
	v_lshlrev_b32_e32 v208, 16, v174
	v_and_b32_e32 v209, 0xffff0000, v174
	v_lshlrev_b32_e32 v174, 16, v175
	v_and_b32_e32 v175, 0xffff0000, v175
	v_pk_add_f32 v[128:129], v[128:129], v[174:175]
	v_lshlrev_b32_e32 v174, 16, v176
	v_and_b32_e32 v175, 0xffff0000, v176
	v_lshlrev_b32_e32 v176, 16, v177
	v_and_b32_e32 v177, 0xffff0000, v177
	v_pk_add_f32 v[126:127], v[126:127], v[208:209]
	v_pk_add_f32 v[176:177], v[124:125], v[176:177]
	v_pk_add_f32 v[124:125], v[122:123], v[174:175]
	v_cvt_pk_bf16_f32 v122, v126, v127
	v_cvt_pk_bf16_f32 v123, v128, v129
	v_cvt_pk_bf16_f32 v124, v124, v125
	v_cvt_pk_bf16_f32 v125, v176, v177
	global_store_dwordx4 v[178:179], v[122:125], off
	s_nop 1
	v_lshlrev_b32_e32 v122, 16, v200
	v_and_b32_e32 v123, 0xffff0000, v200
	v_lshlrev_b32_e32 v124, 16, v201
	v_and_b32_e32 v125, 0xffff0000, v201
	v_pk_add_f32 v[120:121], v[120:121], v[124:125]
	v_pk_add_f32 v[118:119], v[118:119], v[122:123]
	v_lshlrev_b32_e32 v122, 16, v202
	v_and_b32_e32 v123, 0xffff0000, v202
	v_lshlrev_b32_e32 v124, 16, v203
	v_and_b32_e32 v125, 0xffff0000, v203
	v_pk_add_f32 v[124:125], v[116:117], v[124:125]
	v_pk_add_f32 v[116:117], v[114:115], v[122:123]
	v_cvt_pk_bf16_f32 v114, v118, v119
	v_cvt_pk_bf16_f32 v115, v120, v121
	v_cvt_pk_bf16_f32 v116, v116, v117
	v_cvt_pk_bf16_f32 v117, v124, v125
	global_store_dwordx4 v[178:179], v[114:117], off offset:256
	s_nop 1
	v_lshlrev_b32_e32 v114, 16, v204
	v_and_b32_e32 v115, 0xffff0000, v204
	v_lshlrev_b32_e32 v116, 16, v205
	v_and_b32_e32 v117, 0xffff0000, v205
	v_pk_add_f32 v[112:113], v[112:113], v[116:117]
	v_pk_add_f32 v[110:111], v[110:111], v[114:115]
	v_lshlrev_b32_e32 v114, 16, v206
	v_and_b32_e32 v115, 0xffff0000, v206
	v_lshlrev_b32_e32 v116, 16, v207
	v_and_b32_e32 v117, 0xffff0000, v207
	v_pk_add_f32 v[116:117], v[108:109], v[116:117]
	v_pk_add_f32 v[108:109], v[106:107], v[114:115]
	v_cvt_pk_bf16_f32 v106, v110, v111
	v_cvt_pk_bf16_f32 v107, v112, v113
	v_cvt_pk_bf16_f32 v108, v108, v109
	v_cvt_pk_bf16_f32 v109, v116, v117
	global_store_dwordx4 v[168:169], v[106:109], off
	s_nop 1
	v_lshlrev_b32_e32 v106, 16, v146
	v_and_b32_e32 v107, 0xffff0000, v146
	v_lshlrev_b32_e32 v108, 16, v147
	v_and_b32_e32 v109, 0xffff0000, v147
	v_pk_add_f32 v[104:105], v[104:105], v[108:109]
	v_pk_add_f32 v[102:103], v[102:103], v[106:107]
	v_lshlrev_b32_e32 v106, 16, v148
	v_and_b32_e32 v107, 0xffff0000, v148
	v_lshlrev_b32_e32 v108, 16, v149
	v_and_b32_e32 v109, 0xffff0000, v149
	v_pk_add_f32 v[108:109], v[96:97], v[108:109]
	v_pk_add_f32 v[96:97], v[94:95], v[106:107]
	v_cvt_pk_bf16_f32 v94, v102, v103
	v_cvt_pk_bf16_f32 v95, v104, v105
	v_cvt_pk_bf16_f32 v96, v96, v97
	v_cvt_pk_bf16_f32 v97, v108, v109
	global_store_dwordx4 v[168:169], v[94:97], off offset:256
	s_nop 1
	v_lshlrev_b32_e32 v94, 16, v142
	v_and_b32_e32 v95, 0xffff0000, v142
	v_lshlrev_b32_e32 v96, 16, v143
	v_and_b32_e32 v97, 0xffff0000, v143
	v_pk_add_f32 v[96:97], v[100:101], v[96:97]
	v_pk_add_f32 v[94:95], v[98:99], v[94:95]
	v_lshlrev_b32_e32 v98, 16, v144
	v_and_b32_e32 v99, 0xffff0000, v144
	v_lshlrev_b32_e32 v100, 16, v145
	v_and_b32_e32 v101, 0xffff0000, v145
	v_pk_add_f32 v[100:101], v[92:93], v[100:101]
	v_pk_add_f32 v[92:93], v[90:91], v[98:99]
	v_cvt_pk_bf16_f32 v90, v94, v95
	v_cvt_pk_bf16_f32 v91, v96, v97
	v_cvt_pk_bf16_f32 v92, v92, v93
	v_cvt_pk_bf16_f32 v93, v100, v101
	global_store_dwordx4 v[166:167], v[90:93], off
	s_nop 1
	v_lshlrev_b32_e32 v90, 16, v138
	v_and_b32_e32 v91, 0xffff0000, v138
	v_lshlrev_b32_e32 v92, 16, v139
	v_and_b32_e32 v93, 0xffff0000, v139
	v_pk_add_f32 v[84:85], v[84:85], v[92:93]
	v_pk_add_f32 v[82:83], v[82:83], v[90:91]
	v_lshlrev_b32_e32 v90, 16, v140
	v_and_b32_e32 v91, 0xffff0000, v140
	v_lshlrev_b32_e32 v92, 16, v141
	v_and_b32_e32 v93, 0xffff0000, v141
	v_pk_add_f32 v[92:93], v[76:77], v[92:93]
	v_pk_add_f32 v[76:77], v[74:75], v[90:91]
	v_cvt_pk_bf16_f32 v74, v82, v83
	v_cvt_pk_bf16_f32 v75, v84, v85
	v_cvt_pk_bf16_f32 v76, v76, v77
	v_cvt_pk_bf16_f32 v77, v92, v93
	global_store_dwordx4 v[166:167], v[74:77], off offset:256
	v_lshlrev_b32_e32 v82, 16, v136
	v_and_b32_e32 v83, 0xffff0000, v136
	v_lshlrev_b32_e32 v74, 16, v134
	v_and_b32_e32 v75, 0xffff0000, v134
	v_lshlrev_b32_e32 v76, 16, v135
	v_and_b32_e32 v77, 0xffff0000, v135
	v_lshlrev_b32_e32 v84, 16, v137
	v_and_b32_e32 v85, 0xffff0000, v137
	v_pk_add_f32 v[76:77], v[88:89], v[76:77]
	v_pk_add_f32 v[74:75], v[86:87], v[74:75]
	v_pk_add_f32 v[80:81], v[80:81], v[84:85]
	v_pk_add_f32 v[78:79], v[78:79], v[82:83]
	v_cvt_pk_bf16_f32 v74, v74, v75
	v_cvt_pk_bf16_f32 v75, v76, v77
	v_cvt_pk_bf16_f32 v76, v78, v79
	v_cvt_pk_bf16_f32 v77, v80, v81
	global_store_dwordx4 v[164:165], v[74:77], off
	s_nop 0
	v_lshlrev_b32_e32 v74, 16, v130
	v_and_b32_e32 v75, 0xffff0000, v130
	v_lshlrev_b32_e32 v76, 16, v131
	v_and_b32_e32 v77, 0xffff0000, v131
	v_pk_add_f32 v[72:73], v[72:73], v[76:77]
	v_pk_add_f32 v[70:71], v[70:71], v[74:75]
	v_lshlrev_b32_e32 v74, 16, v132
	v_and_b32_e32 v75, 0xffff0000, v132
	v_lshlrev_b32_e32 v76, 16, v133
	v_and_b32_e32 v77, 0xffff0000, v133
	v_pk_add_f32 v[76:77], v[68:69], v[76:77]
	v_pk_add_f32 v[68:69], v[66:67], v[74:75]
	v_cvt_pk_bf16_f32 v66, v70, v71
	v_cvt_pk_bf16_f32 v67, v72, v73
	v_cvt_pk_bf16_f32 v68, v68, v69
	v_cvt_pk_bf16_f32 v69, v76, v77
	global_store_dwordx4 v[164:165], v[66:69], off offset:256
	s_nop 1
	v_add_u32_e32 v66, 0x80, v158
	v_ashrrev_i32_e32 v67, 31, v66
	v_lshlrev_b64 v[66:67], 11, v[66:67]
	v_lshl_add_u64 v[66:67], s[4:5], 0, v[66:67]
	v_lshl_add_u64 v[70:71], v[66:67], 0, v[160:161]
	s_waitcnt vmcnt(8)
	v_mov_b64_e32 v[66:67], v[210:211]
	v_mov_b64_e32 v[68:69], v[212:213]
	v_mov_b64_e32 v[76:77], v[214:215]
	v_mov_b64_e32 v[78:79], v[216:217]
	v_add_co_u32_e32 v72, vcc, s18, v70
	s_mov_b64 s[18:19], -1
	s_nop 0
	v_addc_co_u32_e32 v73, vcc, 0, v71, vcc
	v_mov_b64_e32 v[80:81], v[218:219]
	v_mov_b64_e32 v[82:83], v[220:221]
	v_mov_b64_e32 v[84:85], v[222:223]
	v_mov_b64_e32 v[86:87], v[224:225]
	v_add_co_u32_e32 v104, vcc, s9, v70
	v_lshlrev_b32_e32 v106, 16, v66
	v_addc_co_u32_e32 v105, vcc, 0, v71, vcc
	v_mov_b64_e32 v[88:89], v[226:227]
	v_mov_b64_e32 v[90:91], v[228:229]
	v_mov_b64_e32 v[92:93], v[230:231]
	v_mov_b64_e32 v[94:95], v[232:233]
	v_add_co_u32_e32 v74, vcc, s11, v70
	v_and_b32_e32 v107, 0xffff0000, v66
	s_nop 0
	v_addc_co_u32_e32 v75, vcc, 0, v71, vcc
	v_mov_b64_e32 v[96:97], v[234:235]
	v_mov_b64_e32 v[98:99], v[236:237]
	v_mov_b64_e32 v[100:101], v[238:239]
	v_mov_b64_e32 v[102:103], v[240:241]
	v_lshlrev_b32_e32 v66, 16, v67
	v_and_b32_e32 v67, 0xffff0000, v67
	v_pk_add_f32 v[64:65], v[64:65], v[66:67]
	v_lshlrev_b32_e32 v66, 16, v68
	v_and_b32_e32 v67, 0xffff0000, v68
	v_lshlrev_b32_e32 v68, 16, v69
	v_and_b32_e32 v69, 0xffff0000, v69
	v_pk_add_f32 v[62:63], v[62:63], v[106:107]
	v_pk_add_f32 v[68:69], v[60:61], v[68:69]
	v_pk_add_f32 v[60:61], v[58:59], v[66:67]
	v_cvt_pk_bf16_f32 v58, v62, v63
	v_cvt_pk_bf16_f32 v59, v64, v65
	v_cvt_pk_bf16_f32 v60, v60, v61
	v_cvt_pk_bf16_f32 v61, v68, v69
	global_store_dwordx4 v[70:71], v[58:61], off
	s_andn2_b64 vcc, exec, s[12:13]
	v_lshlrev_b32_e32 v58, 16, v76
	v_and_b32_e32 v59, 0xffff0000, v76
	v_lshlrev_b32_e32 v60, 16, v77
	v_and_b32_e32 v61, 0xffff0000, v77
	v_pk_add_f32 v[56:57], v[56:57], v[60:61]
	v_pk_add_f32 v[54:55], v[54:55], v[58:59]
	v_lshlrev_b32_e32 v58, 16, v78
	v_and_b32_e32 v59, 0xffff0000, v78
	v_lshlrev_b32_e32 v60, 16, v79
	v_and_b32_e32 v61, 0xffff0000, v79
	v_pk_add_f32 v[60:61], v[48:49], v[60:61]
	v_pk_add_f32 v[48:49], v[46:47], v[58:59]
	v_cvt_pk_bf16_f32 v46, v54, v55
	v_cvt_pk_bf16_f32 v47, v56, v57
	v_cvt_pk_bf16_f32 v48, v48, v49
	v_cvt_pk_bf16_f32 v49, v60, v61
	global_store_dwordx4 v[70:71], v[46:49], off offset:256
	s_nop 0
	v_lshlrev_b32_e32 v46, 16, v80
	v_and_b32_e32 v47, 0xffff0000, v80
	v_lshlrev_b32_e32 v48, 16, v81
	v_and_b32_e32 v49, 0xffff0000, v81
	v_pk_add_f32 v[48:49], v[52:53], v[48:49]
	v_pk_add_f32 v[46:47], v[50:51], v[46:47]
	v_lshlrev_b32_e32 v50, 16, v82
	v_and_b32_e32 v51, 0xffff0000, v82
	v_lshlrev_b32_e32 v52, 16, v83
	v_and_b32_e32 v53, 0xffff0000, v83
	v_pk_add_f32 v[52:53], v[44:45], v[52:53]
	v_pk_add_f32 v[44:45], v[42:43], v[50:51]
	v_cvt_pk_bf16_f32 v42, v46, v47
	v_cvt_pk_bf16_f32 v43, v48, v49
	v_cvt_pk_bf16_f32 v44, v44, v45
	v_cvt_pk_bf16_f32 v45, v52, v53
	global_store_dwordx4 v[72:73], v[42:45], off
	s_nop 0
	v_lshlrev_b32_e32 v42, 16, v84
	v_and_b32_e32 v43, 0xffff0000, v84
	v_lshlrev_b32_e32 v44, 16, v85
	v_and_b32_e32 v45, 0xffff0000, v85
	v_pk_add_f32 v[40:41], v[40:41], v[44:45]
	v_pk_add_f32 v[38:39], v[38:39], v[42:43]
	v_lshlrev_b32_e32 v42, 16, v86
	v_and_b32_e32 v43, 0xffff0000, v86
	v_lshlrev_b32_e32 v44, 16, v87
	v_and_b32_e32 v45, 0xffff0000, v87
	v_pk_add_f32 v[44:45], v[32:33], v[44:45]
	v_pk_add_f32 v[32:33], v[30:31], v[42:43]
	v_cvt_pk_bf16_f32 v30, v38, v39
	v_cvt_pk_bf16_f32 v31, v40, v41
	v_cvt_pk_bf16_f32 v32, v32, v33
	v_cvt_pk_bf16_f32 v33, v44, v45
	global_store_dwordx4 v[72:73], v[30:33], off offset:256
	s_nop 0
	v_lshlrev_b32_e32 v30, 16, v88
	v_and_b32_e32 v31, 0xffff0000, v88
	v_lshlrev_b32_e32 v32, 16, v89
	v_and_b32_e32 v33, 0xffff0000, v89
	v_pk_add_f32 v[32:33], v[36:37], v[32:33]
	v_pk_add_f32 v[30:31], v[34:35], v[30:31]
	v_lshlrev_b32_e32 v34, 16, v90
	v_and_b32_e32 v35, 0xffff0000, v90
	v_lshlrev_b32_e32 v36, 16, v91
	v_and_b32_e32 v37, 0xffff0000, v91
	v_pk_add_f32 v[36:37], v[28:29], v[36:37]
	v_pk_add_f32 v[28:29], v[26:27], v[34:35]
	v_cvt_pk_bf16_f32 v26, v30, v31
	v_cvt_pk_bf16_f32 v27, v32, v33
	v_cvt_pk_bf16_f32 v28, v28, v29
	v_cvt_pk_bf16_f32 v29, v36, v37
	global_store_dwordx4 v[104:105], v[26:29], off
	s_nop 0
	v_lshlrev_b32_e32 v26, 16, v92
	v_and_b32_e32 v27, 0xffff0000, v92
	v_lshlrev_b32_e32 v28, 16, v93
	v_and_b32_e32 v29, 0xffff0000, v93
	v_pk_add_f32 v[24:25], v[24:25], v[28:29]
	v_pk_add_f32 v[22:23], v[22:23], v[26:27]
	v_lshlrev_b32_e32 v26, 16, v94
	v_and_b32_e32 v27, 0xffff0000, v94
	v_lshlrev_b32_e32 v28, 16, v95
	v_and_b32_e32 v29, 0xffff0000, v95
	v_pk_add_f32 v[28:29], v[16:17], v[28:29]
	v_pk_add_f32 v[16:17], v[14:15], v[26:27]
	v_cvt_pk_bf16_f32 v14, v22, v23
	v_cvt_pk_bf16_f32 v15, v24, v25
	v_cvt_pk_bf16_f32 v16, v16, v17
	v_cvt_pk_bf16_f32 v17, v28, v29
	global_store_dwordx4 v[104:105], v[14:17], off offset:256
	s_nop 0
	v_lshlrev_b32_e32 v14, 16, v96
	v_and_b32_e32 v15, 0xffff0000, v96
	v_lshlrev_b32_e32 v16, 16, v97
	v_and_b32_e32 v17, 0xffff0000, v97
	v_pk_add_f32 v[16:17], v[20:21], v[16:17]
	v_pk_add_f32 v[14:15], v[18:19], v[14:15]
	v_lshlrev_b32_e32 v18, 16, v98
	v_and_b32_e32 v19, 0xffff0000, v98
	v_lshlrev_b32_e32 v20, 16, v99
	v_and_b32_e32 v21, 0xffff0000, v99
	v_pk_add_f32 v[20:21], v[12:13], v[20:21]
	v_pk_add_f32 v[12:13], v[10:11], v[18:19]
	v_cvt_pk_bf16_f32 v10, v14, v15
	v_cvt_pk_bf16_f32 v11, v16, v17
	v_cvt_pk_bf16_f32 v12, v12, v13
	v_cvt_pk_bf16_f32 v13, v20, v21
	global_store_dwordx4 v[74:75], v[10:13], off
	s_nop 0
	v_lshlrev_b32_e32 v10, 16, v100
	v_and_b32_e32 v11, 0xffff0000, v100
	v_lshlrev_b32_e32 v12, 16, v101
	v_and_b32_e32 v13, 0xffff0000, v101
	v_pk_add_f32 v[8:9], v[8:9], v[12:13]
	v_pk_add_f32 v[6:7], v[6:7], v[10:11]
	v_lshlrev_b32_e32 v10, 16, v102
	v_and_b32_e32 v11, 0xffff0000, v102
	v_lshlrev_b32_e32 v12, 16, v103
	v_and_b32_e32 v13, 0xffff0000, v103
	v_pk_add_f32 v[12:13], v[4:5], v[12:13]
	v_pk_add_f32 v[4:5], v[2:3], v[10:11]
	v_cvt_pk_bf16_f32 v2, v6, v7
	v_cvt_pk_bf16_f32 v3, v8, v9
	v_cvt_pk_bf16_f32 v4, v4, v5
	v_cvt_pk_bf16_f32 v5, v12, v13
	global_store_dwordx4 v[74:75], v[2:5], off offset:256
	s_cbranch_vccnz .LBB0_988
	s_andn2_b64 vcc, exec, s[0:1]
	s_cbranch_vccnz .LBB0_987
	s_barrier
	s_branch .LBB0_987
